# P2: PROJ tile stores non-temporal
# speedup vs baseline: 1.0133x; 1.0133x over previous
.LBB0_1095:
	s_movk_i32 s17, 0x100
	s_nop 15
	s_nop 7
	v_mov_b32_e32 v3, v1
	v_mov_b32_e32 v4, v186
	s_cmp_lt_i32 s53, 4
	s_cselect_b64 vcc, -1, 0
	v_cndmask_b32_e32 v2, v204, v205, vcc
	v_add_u32_e32 v6, s40, v3
	v_lshlrev_b32_e32 v4, 3, v4
	v_ashrrev_i32_e32 v5, 31, v4
	v_mov_b32_e32 v3, v2
	v_cmp_gt_i32_e32 vcc, s17, v6
	s_and_saveexec_b64 s[24:25], vcc
	s_cbranch_execz .LBB0_1097
	v_add_u32_e32 v7, s6, v6
	v_mov_b64_e32 v[8:9], s[96:97]
	v_mad_i64_i32 v[8:9], s[26:27], v7, s51, v[8:9]
	s_lshl_b32 s26, s53, 8
	s_ashr_i32 s27, s26, 31
	v_lshl_add_u64 v[8:9], s[26:27], 1, v[8:9]
	s_lshl_b32 s8, s41, 1
	v_lshl_add_u64 v[8:9], v[8:9], 0, s[8:9]
	v_mov_b32_e32 v14, v2
	v_mov_b32_e32 v15, v2
	v_lshl_add_u64 v[12:13], v[4:5], 1, v[8:9]
	v_pk_mul_f32 v[10:11], v[160:161], v[14:15]
	v_pk_mul_f32 v[8:9], v[158:159], v[2:3]
	v_pk_mul_f32 v[16:17], v[156:157], v[14:15]
	v_pk_mul_f32 v[18:19], v[154:155], v[2:3]
	v_cvt_pk_bf16_f32 v8, v8, v9
	v_cvt_pk_bf16_f32 v9, v10, v11
	s_nop 0
	v_cvt_pk_bf16_f32 v10, v18, v19
	v_cvt_pk_bf16_f32 v11, v16, v17
	global_store_dwordx4 v[12:13], v[8:11], off nt
	v_pk_mul_f32 v[16:17], v[146:147], v[2:3]
	s_nop 0
	v_pk_mul_f32 v[10:11], v[152:153], v[14:15]
	v_pk_mul_f32 v[8:9], v[150:151], v[2:3]
	v_pk_mul_f32 v[14:15], v[148:149], v[14:15]
	v_cvt_pk_bf16_f32 v8, v8, v9
	v_cvt_pk_bf16_f32 v9, v10, v11
	v_cvt_pk_bf16_f32 v10, v16, v17
	s_nop 0
	v_cvt_pk_bf16_f32 v11, v14, v15
	global_store_dwordx4 v[12:13], v[8:11], off offset:256 nt
.LBB0_1097:
	s_or_b64 exec, exec, s[24:25]
	v_add_u32_e32 v7, 16, v6
	v_cmp_gt_i32_e32 vcc, s17, v7
	s_and_saveexec_b64 s[24:25], vcc
	s_cbranch_execz .LBB0_1099
	v_add_u32_e32 v7, s6, v7
	v_mov_b64_e32 v[8:9], s[96:97]
	v_mad_i64_i32 v[8:9], s[26:27], v7, s51, v[8:9]
	s_lshl_b32 s26, s53, 8
	s_ashr_i32 s27, s26, 31
	v_lshl_add_u64 v[8:9], s[26:27], 1, v[8:9]
	s_lshl_b32 s8, s41, 1
	v_lshl_add_u64 v[8:9], v[8:9], 0, s[8:9]
	v_mov_b32_e32 v14, v2
	v_mov_b32_e32 v15, v2
	v_lshl_add_u64 v[12:13], v[4:5], 1, v[8:9]
	v_pk_mul_f32 v[10:11], v[144:145], v[14:15]
	v_pk_mul_f32 v[8:9], v[142:143], v[2:3]
	v_pk_mul_f32 v[16:17], v[140:141], v[14:15]
	v_pk_mul_f32 v[18:19], v[138:139], v[2:3]
	v_cvt_pk_bf16_f32 v8, v8, v9
	v_cvt_pk_bf16_f32 v9, v10, v11
	s_nop 0
	v_cvt_pk_bf16_f32 v10, v18, v19
	v_cvt_pk_bf16_f32 v11, v16, v17
	global_store_dwordx4 v[12:13], v[8:11], off nt
	v_pk_mul_f32 v[16:17], v[130:131], v[2:3]
	s_nop 0
	v_pk_mul_f32 v[10:11], v[136:137], v[14:15]
	v_pk_mul_f32 v[8:9], v[134:135], v[2:3]
	v_pk_mul_f32 v[14:15], v[132:133], v[14:15]
	v_cvt_pk_bf16_f32 v8, v8, v9
	v_cvt_pk_bf16_f32 v9, v10, v11
	v_cvt_pk_bf16_f32 v10, v16, v17
	s_nop 0
	v_cvt_pk_bf16_f32 v11, v14, v15
	global_store_dwordx4 v[12:13], v[8:11], off offset:256 nt
.LBB0_1099:
	s_or_b64 exec, exec, s[24:25]
	v_add_u32_e32 v7, 32, v6
	v_cmp_gt_i32_e32 vcc, s17, v7
	s_and_saveexec_b64 s[24:25], vcc
	s_cbranch_execz .LBB0_1101
	v_add_u32_e32 v7, s6, v7
	v_mov_b64_e32 v[8:9], s[96:97]
	v_mad_i64_i32 v[8:9], s[26:27], v7, s51, v[8:9]
	s_lshl_b32 s26, s53, 8
	s_ashr_i32 s27, s26, 31
	v_lshl_add_u64 v[8:9], s[26:27], 1, v[8:9]
	s_lshl_b32 s8, s41, 1
	v_lshl_add_u64 v[8:9], v[8:9], 0, s[8:9]
	v_mov_b32_e32 v14, v2
	v_mov_b32_e32 v15, v2
	v_lshl_add_u64 v[12:13], v[4:5], 1, v[8:9]
	v_pk_mul_f32 v[10:11], v[128:129], v[14:15]
	v_pk_mul_f32 v[8:9], v[126:127], v[2:3]
	v_pk_mul_f32 v[16:17], v[124:125], v[14:15]
	v_pk_mul_f32 v[18:19], v[122:123], v[2:3]
	v_cvt_pk_bf16_f32 v8, v8, v9
	v_cvt_pk_bf16_f32 v9, v10, v11
	s_nop 0
	v_cvt_pk_bf16_f32 v10, v18, v19
	v_cvt_pk_bf16_f32 v11, v16, v17
	global_store_dwordx4 v[12:13], v[8:11], off nt
	v_pk_mul_f32 v[16:17], v[114:115], v[2:3]
	s_nop 0
	v_pk_mul_f32 v[10:11], v[120:121], v[14:15]
	v_pk_mul_f32 v[8:9], v[118:119], v[2:3]
	v_pk_mul_f32 v[14:15], v[116:117], v[14:15]
	v_cvt_pk_bf16_f32 v8, v8, v9
	v_cvt_pk_bf16_f32 v9, v10, v11
	v_cvt_pk_bf16_f32 v10, v16, v17
	s_nop 0
	v_cvt_pk_bf16_f32 v11, v14, v15
	global_store_dwordx4 v[12:13], v[8:11], off offset:256 nt
.LBB0_1101:
	s_or_b64 exec, exec, s[24:25]
	v_add_u32_e32 v7, 48, v6
	v_cmp_gt_i32_e32 vcc, s17, v7
	s_and_saveexec_b64 s[24:25], vcc
	s_cbranch_execz .LBB0_1103
	v_add_u32_e32 v7, s6, v7
	v_mov_b64_e32 v[8:9], s[96:97]
	v_mad_i64_i32 v[8:9], s[26:27], v7, s51, v[8:9]
	s_lshl_b32 s26, s53, 8
	s_ashr_i32 s27, s26, 31
	v_lshl_add_u64 v[8:9], s[26:27], 1, v[8:9]
	s_lshl_b32 s8, s41, 1
	v_lshl_add_u64 v[8:9], v[8:9], 0, s[8:9]
	v_mov_b32_e32 v14, v2
	v_mov_b32_e32 v15, v2
	v_lshl_add_u64 v[12:13], v[4:5], 1, v[8:9]
	v_pk_mul_f32 v[10:11], v[112:113], v[14:15]
	v_pk_mul_f32 v[8:9], v[110:111], v[2:3]
	v_pk_mul_f32 v[16:17], v[108:109], v[14:15]
	v_pk_mul_f32 v[18:19], v[106:107], v[2:3]
	v_cvt_pk_bf16_f32 v8, v8, v9
	v_cvt_pk_bf16_f32 v9, v10, v11
	s_nop 0
	v_cvt_pk_bf16_f32 v10, v18, v19
	v_cvt_pk_bf16_f32 v11, v16, v17
	global_store_dwordx4 v[12:13], v[8:11], off nt
	v_pk_mul_f32 v[16:17], v[98:99], v[2:3]
	s_nop 0
	v_pk_mul_f32 v[10:11], v[104:105], v[14:15]
	v_pk_mul_f32 v[8:9], v[102:103], v[2:3]
	v_pk_mul_f32 v[14:15], v[100:101], v[14:15]
	v_cvt_pk_bf16_f32 v8, v8, v9
	v_cvt_pk_bf16_f32 v9, v10, v11
	v_cvt_pk_bf16_f32 v10, v16, v17
	s_nop 0
	v_cvt_pk_bf16_f32 v11, v14, v15
	global_store_dwordx4 v[12:13], v[8:11], off offset:256 nt
.LBB0_1103:
	s_or_b64 exec, exec, s[24:25]
	v_add_u32_e32 v7, 0x80, v6
	v_cmp_gt_i32_e32 vcc, s17, v7
	s_and_saveexec_b64 s[24:25], vcc
	s_cbranch_execz .LBB0_1105
	v_add_u32_e32 v7, s6, v7
	v_mov_b64_e32 v[8:9], s[96:97]
	v_mad_i64_i32 v[8:9], s[26:27], v7, s51, v[8:9]
	s_lshl_b32 s26, s53, 8
	s_ashr_i32 s27, s26, 31
	v_lshl_add_u64 v[8:9], s[26:27], 1, v[8:9]
	s_lshl_b32 s8, s41, 1
	v_lshl_add_u64 v[8:9], v[8:9], 0, s[8:9]
	v_mov_b32_e32 v14, v2
	v_mov_b32_e32 v15, v2
	v_lshl_add_u64 v[12:13], v[4:5], 1, v[8:9]
	v_pk_mul_f32 v[10:11], v[96:97], v[14:15]
	v_pk_mul_f32 v[8:9], v[94:95], v[2:3]
	v_pk_mul_f32 v[16:17], v[92:93], v[14:15]
	v_pk_mul_f32 v[18:19], v[90:91], v[2:3]
	v_cvt_pk_bf16_f32 v8, v8, v9
	v_cvt_pk_bf16_f32 v9, v10, v11
	s_nop 0
	v_cvt_pk_bf16_f32 v10, v18, v19
	v_cvt_pk_bf16_f32 v11, v16, v17
	global_store_dwordx4 v[12:13], v[8:11], off nt
	v_pk_mul_f32 v[16:17], v[82:83], v[2:3]
	s_nop 0
	v_pk_mul_f32 v[10:11], v[88:89], v[14:15]
	v_pk_mul_f32 v[8:9], v[86:87], v[2:3]
	v_pk_mul_f32 v[14:15], v[84:85], v[14:15]
	v_cvt_pk_bf16_f32 v8, v8, v9
	v_cvt_pk_bf16_f32 v9, v10, v11
	v_cvt_pk_bf16_f32 v10, v16, v17
	s_nop 0
	v_cvt_pk_bf16_f32 v11, v14, v15
	global_store_dwordx4 v[12:13], v[8:11], off offset:256 nt
.LBB0_1105:
	s_or_b64 exec, exec, s[24:25]
	v_add_u32_e32 v7, 0x90, v6
	v_cmp_gt_i32_e32 vcc, s17, v7
	s_and_saveexec_b64 s[24:25], vcc
	s_cbranch_execz .LBB0_1107
	v_add_u32_e32 v7, s6, v7
	v_mov_b64_e32 v[8:9], s[96:97]
	v_mad_i64_i32 v[8:9], s[26:27], v7, s51, v[8:9]
	s_lshl_b32 s26, s53, 8
	s_ashr_i32 s27, s26, 31
	v_lshl_add_u64 v[8:9], s[26:27], 1, v[8:9]
	s_lshl_b32 s8, s41, 1
	v_lshl_add_u64 v[8:9], v[8:9], 0, s[8:9]
	v_mov_b32_e32 v14, v2
	v_mov_b32_e32 v15, v2
	v_lshl_add_u64 v[12:13], v[4:5], 1, v[8:9]
	v_pk_mul_f32 v[10:11], v[80:81], v[14:15]
	v_pk_mul_f32 v[8:9], v[78:79], v[2:3]
	v_pk_mul_f32 v[16:17], v[76:77], v[14:15]
	v_pk_mul_f32 v[18:19], v[74:75], v[2:3]
	v_cvt_pk_bf16_f32 v8, v8, v9
	v_cvt_pk_bf16_f32 v9, v10, v11
	s_nop 0
	v_cvt_pk_bf16_f32 v10, v18, v19
	v_cvt_pk_bf16_f32 v11, v16, v17
	global_store_dwordx4 v[12:13], v[8:11], off nt
	v_pk_mul_f32 v[16:17], v[66:67], v[2:3]
	s_nop 0
	v_pk_mul_f32 v[10:11], v[72:73], v[14:15]
	v_pk_mul_f32 v[8:9], v[70:71], v[2:3]
	v_pk_mul_f32 v[14:15], v[68:69], v[14:15]
	v_cvt_pk_bf16_f32 v8, v8, v9
	v_cvt_pk_bf16_f32 v9, v10, v11
	v_cvt_pk_bf16_f32 v10, v16, v17
	s_nop 0
	v_cvt_pk_bf16_f32 v11, v14, v15
	global_store_dwordx4 v[12:13], v[8:11], off offset:256 nt
.LBB0_1107:
	s_or_b64 exec, exec, s[24:25]
	v_add_u32_e32 v7, 0xa0, v6
	v_cmp_gt_i32_e32 vcc, s17, v7
	s_and_saveexec_b64 s[24:25], vcc
	s_cbranch_execz .LBB0_1109
	v_add_u32_e32 v7, s6, v7
	v_mov_b64_e32 v[8:9], s[96:97]
	v_mad_i64_i32 v[8:9], s[26:27], v7, s51, v[8:9]
	s_lshl_b32 s26, s53, 8
	s_ashr_i32 s27, s26, 31
	v_lshl_add_u64 v[8:9], s[26:27], 1, v[8:9]
	s_lshl_b32 s8, s41, 1
	v_lshl_add_u64 v[8:9], v[8:9], 0, s[8:9]
	v_mov_b32_e32 v14, v2
	v_mov_b32_e32 v15, v2
	v_lshl_add_u64 v[12:13], v[4:5], 1, v[8:9]
	v_pk_mul_f32 v[10:11], v[64:65], v[14:15]
	v_pk_mul_f32 v[8:9], v[62:63], v[2:3]
	v_pk_mul_f32 v[16:17], v[60:61], v[14:15]
	v_pk_mul_f32 v[18:19], v[58:59], v[2:3]
	v_cvt_pk_bf16_f32 v8, v8, v9
	v_cvt_pk_bf16_f32 v9, v10, v11
	s_nop 0
	v_cvt_pk_bf16_f32 v10, v18, v19
	v_cvt_pk_bf16_f32 v11, v16, v17
	global_store_dwordx4 v[12:13], v[8:11], off nt
	v_pk_mul_f32 v[16:17], v[50:51], v[2:3]
	s_nop 0
	v_pk_mul_f32 v[10:11], v[56:57], v[14:15]
	v_pk_mul_f32 v[8:9], v[54:55], v[2:3]
	v_pk_mul_f32 v[14:15], v[52:53], v[14:15]
	v_cvt_pk_bf16_f32 v8, v8, v9
	v_cvt_pk_bf16_f32 v9, v10, v11
	v_cvt_pk_bf16_f32 v10, v16, v17
	s_nop 0
	v_cvt_pk_bf16_f32 v11, v14, v15
	global_store_dwordx4 v[12:13], v[8:11], off offset:256 nt
.LBB0_1109:
	s_or_b64 exec, exec, s[24:25]
	v_add_u32_e32 v6, 0xb0, v6
	v_cmp_gt_i32_e32 vcc, s17, v6
	s_and_saveexec_b64 s[24:25], vcc
	s_cbranch_execz .LBB0_1111
	v_add_u32_e32 v8, s6, v6
	v_mov_b64_e32 v[6:7], s[96:97]
	v_mad_i64_i32 v[6:7], s[26:27], v8, s51, v[6:7]
	s_lshl_b32 s26, s53, 8
	s_ashr_i32 s27, s26, 31
	v_lshl_add_u64 v[6:7], s[26:27], 1, v[6:7]
	s_lshl_b32 s8, s41, 1
	v_lshl_add_u64 v[6:7], v[6:7], 0, s[8:9]
	v_lshl_add_u64 v[8:9], v[4:5], 1, v[6:7]
	v_mov_b32_e32 v10, v2
	v_mov_b32_e32 v11, v2
	v_pk_mul_f32 v[4:5], v[46:47], v[2:3]
	v_pk_mul_f32 v[6:7], v[48:49], v[10:11]
	v_cvt_pk_bf16_f32 v4, v4, v5
	v_pk_mul_f32 v[12:13], v[44:45], v[10:11]
	v_cvt_pk_bf16_f32 v5, v6, v7
	v_pk_mul_f32 v[14:15], v[42:43], v[2:3]
	s_nop 0
	v_cvt_pk_bf16_f32 v6, v14, v15
	v_cvt_pk_bf16_f32 v7, v12, v13
	global_store_dwordx4 v[8:9], v[4:7], off nt
	v_pk_mul_f32 v[12:13], v[34:35], v[2:3]
	s_nop 0
	v_pk_mul_f32 v[4:5], v[40:41], v[10:11]
	v_pk_mul_f32 v[6:7], v[38:39], v[2:3]
	v_pk_mul_f32 v[10:11], v[36:37], v[10:11]
	v_cvt_pk_bf16_f32 v2, v6, v7
	v_cvt_pk_bf16_f32 v3, v4, v5
	v_cvt_pk_bf16_f32 v4, v12, v13
	s_nop 0
	v_cvt_pk_bf16_f32 v5, v10, v11
	global_store_dwordx4 v[8:9], v[2:5], off offset:256 nt
